# speedup vs baseline: 1.0357x; 1.0012x over previous
_ZN4attn8attn_fwdEPKDF16_PDF16_:
	s_mov_b32 s91, 0
	s_mov_b64 s[88:89], s[0:1]
	s_mov_b32 s87, s2
.Lattn_unit:
	s_load_dwordx4 s[4:7], s[0:1], 0x0
	s_lshr_b32 s0, s2, 2
	s_and_b32 s3, s2, 7
	s_and_b32 s0, s0, 8
	s_or_b32 s30, s0, s3
	s_lshr_b32 s18, s2, 6
	s_mov_b32 s19, 0
	s_lshl_b32 s0, s2, 5
	v_readfirstlane_b32 s16, v0
	s_and_b32 s12, s0, 0x300
	s_xor_b32 s12, s12, s91
	s_lshl_b64 s[8:9], s[18:19], 15
	s_lshl_b32 s0, s30, 11
	s_lshr_b32 s33, s16, 6
	s_or_b32 s8, s8, s0
	s_or_b32 s0, s8, s12
	s_lshl_b32 s31, s33, 5
	s_add_u32 s0, s0, s31
	s_addc_u32 s1, s9, 0
	s_lshl_b64 s[0:1], s[0:1], 7
	s_waitcnt lgkmcnt(0)
	s_add_u32 s0, s4, s0
	s_addc_u32 s1, s5, s1
	s_lshl_b64 s[10:11], s[8:9], 7
	v_bfe_u32 v190, v0, 3, 3
	s_add_u32 s10, s4, s10
	v_lshl_or_b32 v182, s33, 3, v190
	s_addc_u32 s11, s5, s11
	v_lshrrev_b32_e32 v89, 1, v182
	s_add_u32 s14, s10, 0x1000000
	v_xor_b32_e32 v4, v89, v0
	s_addc_u32 s15, s11, 0
	v_mov_b32_e32 v183, 0
	v_lshlrev_b32_e32 v4, 4, v4
	s_add_u32 s10, s10, 0x2000000
	v_lshlrev_b64 v[86:87], 7, v[182:183]
	v_and_b32_e32 v1, 7, v0
	v_and_b32_e32 v182, 0x70, v4
	v_lshrrev_b32_e32 v4, 2, v0
	s_addc_u32 s11, s11, 0
	v_lshl_add_u64 v[2:3], s[14:15], 0, v[86:87]
	v_bitop3_b32 v4, v4, v1, 4 bitop3:0x6c
	v_lshl_add_u64 v[186:187], v[2:3], 0, v[182:183]
	v_lshl_add_u64 v[2:3], s[10:11], 0, v[86:87]
	v_lshlrev_b32_e32 v182, 4, v4
	s_lshl_b32 s36, s33, 10
	s_mov_b32 s13, m0
	s_mov_b32 m0, s36
	s_nop 0
	global_load_lds_dwordx4 v[186:187], off
	s_mov_b32 m0, s13
	s_mov_b64 s[20:21], 0x2000
	v_and_b32_e32 v191, 31, v0
	v_lshl_add_u64 v[194:195], v[2:3], 0, v[182:183]
	s_add_i32 s35, s36, 0x6000
	s_mov_b32 s13, m0
	s_mov_b32 m0, s35
	s_nop 0
	global_load_lds_dwordx4 v[194:195], off
	s_mov_b32 m0, s13
	v_lshl_add_u64 v[2:3], v[186:187], 0, s[20:21]
	v_bfe_u32 v88, v0, 5, 1
	s_add_i32 s37, s36, 0x2000
	s_mov_b32 s13, m0
	s_mov_b32 m0, s37
	s_nop 0
	global_load_lds_dwordx4 v[2:3], off
	s_mov_b32 m0, s13
	v_lshlrev_b32_e32 v2, 6, v191
	v_lshl_or_b32 v192, v88, 3, v2
	v_lshlrev_b32_e32 v14, 1, v192
	global_load_dwordx4 v[154:157], v14, s[0:1]
	global_load_dwordx4 v[146:149], v14, s[0:1] offset:32
	global_load_dwordx4 v[138:141], v14, s[0:1] offset:64
	global_load_dwordx4 v[134:137], v14, s[0:1] offset:96
	v_lshrrev_b32_e32 v18, 1, v0
	s_mov_b64 s[22:23], 0x4000
	v_mov_b32_e32 v2, v183
	v_mov_b32_e32 v3, v183
	v_mov_b32_e32 v4, v183
	v_mov_b32_e32 v5, v183
	v_mov_b32_e32 v6, v183
	v_mov_b32_e32 v7, v183
	v_mov_b32_e32 v8, v183
	v_mov_b32_e32 v9, v183
	v_mov_b32_e32 v10, v183
	v_mov_b32_e32 v11, v183
	v_mov_b32_e32 v12, v183
	v_mov_b32_e32 v13, v183
	v_mov_b32_e32 v14, v183
	v_mov_b32_e32 v15, v183
	v_mov_b32_e32 v16, v183
	v_mov_b32_e32 v17, v183
	v_lshlrev_b32_e32 v38, 7, v191
	v_bitop3_b32 v18, v88, v18, 7 bitop3:0x78
	v_lshl_or_b32 v211, v18, 4, v38
	v_lshl_add_u64 v[18:19], v[186:187], 0, s[22:23]
	s_add_i32 s0, s36, 0x4000
	s_mov_b32 s1, m0
	s_mov_b32 m0, s0
	s_nop 0
	global_load_lds_dwordx4 v[18:19], off
	s_mov_b32 m0, s1
	s_waitcnt vmcnt(3) lgkmcnt(0)
	s_barrier
	ds_read_b128 v[34:37], v211
	v_bfe_u32 v39, v0, 1, 3
	v_bitop3_b32 v40, v88, v39, 2 bitop3:0x36
	v_lshl_or_b32 v210, v40, 4, v38
	v_bitop3_b32 v40, v88, v39, 4 bitop3:0x36
	v_lshl_or_b32 v209, v40, 4, v38
	v_bitop3_b32 v39, v88, v39, 6 bitop3:0x36
	v_lshl_or_b32 v208, v39, 4, v38
	v_lshlrev_b32_e32 v201, 9, v88
	s_and_b32 s0, s16, 0x3fffffc0
	s_mov_b64 s[24:25], 0x6000
	s_lshl_b32 s38, s0, 2
	s_add_i32 s34, s36, 0x8000
	s_lshl_b32 s2, s2, 16
	s_lshl_b32 s3, s3, 18
	s_waitcnt vmcnt(3) lgkmcnt(0)
	v_mfma_f32_32x32x16_f16 v[18:33], v[34:37], v[154:157], v[2:17]
	ds_read_b128 v[34:37], v211 offset:4096
	s_and_b32 s2, s2, 0x200000
	s_lshl_b64 s[16:17], s[18:19], 22
	s_or_b32 s2, s2, s3
	s_or_b32 s16, s16, s2
	s_mov_b64 s[2:3], 0x1002000
	v_and_b32_e32 v90, 63, v0
	s_waitcnt lgkmcnt(0)
	v_mfma_f32_32x32x16_f16 v[2:17], v[34:37], v[154:157], v[2:17]
	ds_read_b128 v[34:37], v210
	s_mov_b32 s13, s19
	s_movk_i32 s42, 0x2000
	s_movk_i32 s39, 0x4000
	v_lshl_or_b32 v204, v191, 2, s38
	v_lshlrev_b32_e32 v212, 4, v88
	s_mov_b32 s40, -1
	s_waitcnt vmcnt(2) lgkmcnt(0)
	v_mfma_f32_32x32x16_f16 v[18:33], v[34:37], v[146:149], v[18:33]
	ds_read_b128 v[34:37], v210 offset:4096
	s_mov_b32 s41, 0x41000000
	s_mov_b32 s26, s19
	s_waitcnt lgkmcnt(0)
	v_mfma_f32_32x32x16_f16 v[2:17], v[34:37], v[146:149], v[2:17]
	ds_read_b128 v[34:37], v209
	s_waitcnt vmcnt(1) lgkmcnt(0)
	v_mfma_f32_32x32x16_f16 v[18:33], v[34:37], v[138:141], v[18:33]
	ds_read_b128 v[34:37], v209 offset:4096
	ds_read_b128 v[38:41], v208 offset:4096
	ds_read_b128 v[42:45], v208
	s_waitcnt lgkmcnt(2)
	v_mfma_f32_32x32x16_f16 v[2:17], v[34:37], v[138:141], v[2:17]
	v_lshlrev_b32_e32 v34, 5, v0
	v_lshlrev_b32_e32 v35, 1, v0
	v_lshlrev_b32_e32 v36, 3, v0
	v_and_b32_e32 v34, 0x180, v34
	v_and_b32_e32 v193, 24, v36
	v_and_or_b32 v34, v35, 32, v34
	v_or3_b32 v203, v34, v193, v201
	s_waitcnt vmcnt(0) lgkmcnt(0)
	v_mfma_f32_32x32x16_f16 v[18:33], v[42:45], v[134:137], v[18:33]
	v_and_b32_e32 v200, 64, v36
	v_bitop3_b32 v202, v36, 64, v36 bitop3:0xc
	v_or_b32_e32 v206, v203, v200
	v_or_b32_e32 v207, v203, v202
	v_mfma_f32_32x32x16_f16 v[2:17], v[38:41], v[134:137], v[2:17]
	s_nop 15
	s_nop 7
	s_nop 0
	v_max3_f32 v34, v18, v19, v2
	v_max3_f32 v35, v20, v21, v3
	s_nop 0
	v_max3_f32 v34, v34, v4, v5
	v_max3_f32 v35, v35, v24, v25
	s_nop 0
	v_max3_f32 v34, v34, v22, v23
	v_max3_f32 v35, v35, v8, v9
	s_nop 0
	v_max3_f32 v34, v34, v6, v7
	v_max3_f32 v35, v35, v28, v29
	s_nop 0
	v_max3_f32 v34, v34, v26, v27
	v_max3_f32 v35, v35, v12, v13
	s_nop 0
	v_max3_f32 v34, v34, v10, v11
	v_max3_f32 v35, v35, v32, v33
	s_nop 0
	v_max3_f32 v34, v34, v30, v31
	v_max3_f32 v35, v35, v16, v17
	s_nop 0
	v_max3_f32 v34, v34, v14, v15
	s_nop 0
	v_max_f32_e32 v34, v34, v35
	s_nop 0
	v_mov_b32_e32 v35, v34
	s_nop 1
	v_permlane32_swap_b32_e32 v34, v35
	v_max_f32_e32 v34, v34, v35
	s_nop 0
	v_add_f32_e32 v205, v183, v34
	v_sub_f32_e32 v18, v18, v34
	v_sub_f32_e32 v2, v2, v34
	v_sub_f32_e32 v19, v19, v34
	v_sub_f32_e32 v3, v3, v34
	v_sub_f32_e32 v20, v20, v34
	v_sub_f32_e32 v4, v4, v34
	v_sub_f32_e32 v21, v21, v34
	v_sub_f32_e32 v5, v5, v34
	v_sub_f32_e32 v22, v22, v34
	v_sub_f32_e32 v6, v6, v34
	v_sub_f32_e32 v23, v23, v34
	v_sub_f32_e32 v7, v7, v34
	v_sub_f32_e32 v24, v24, v34
	v_sub_f32_e32 v8, v8, v34
	v_sub_f32_e32 v25, v25, v34
	v_sub_f32_e32 v9, v9, v34
	v_sub_f32_e32 v26, v26, v34
	v_sub_f32_e32 v10, v10, v34
	v_sub_f32_e32 v27, v27, v34
	v_sub_f32_e32 v11, v11, v34
	v_sub_f32_e32 v28, v28, v34
	v_sub_f32_e32 v12, v12, v34
	v_sub_f32_e32 v29, v29, v34
	v_sub_f32_e32 v13, v13, v34
	v_sub_f32_e32 v30, v30, v34
	v_sub_f32_e32 v14, v14, v34
	v_sub_f32_e32 v31, v31, v34
	v_sub_f32_e32 v15, v15, v34
	v_sub_f32_e32 v32, v32, v34
	v_sub_f32_e32 v16, v16, v34
	v_sub_f32_e32 v33, v33, v34
	v_sub_f32_e32 v17, v17, v34
	s_nop 0
	v_xor_b32_e32 v34, 0x80000000, v205
	v_mov_b32_e32 v35, v34
	v_mov_b32_e32 v36, v34
	v_mov_b32_e32 v37, v34
	v_mov_b32_e32 v38, v34
	v_mov_b32_e32 v39, v34
	v_mov_b32_e32 v40, v34
	v_mov_b32_e32 v41, v34
	v_mov_b32_e32 v42, v34
	v_mov_b32_e32 v43, v34
	v_mov_b32_e32 v44, v34
	v_mov_b32_e32 v45, v34
	v_mov_b32_e32 v46, v34
	v_mov_b32_e32 v47, v34
	v_mov_b32_e32 v48, v34
	v_mov_b32_e32 v49, v34
	s_waitcnt vmcnt(0) lgkmcnt(0)
	s_barrier
	v_exp_f32_e32 v50, v2
	v_exp_f32_e32 v51, v3
	v_lshl_add_u64 v[2:3], v[186:187], 0, s[24:25]
	s_mov_b32 s0, m0
	s_mov_b32 m0, s36
	s_nop 0
	global_load_lds_dwordx4 v[2:3], off
	s_mov_b32 m0, s0
	v_lshl_add_u64 v[2:3], v[194:195], 0, s[20:21]
	s_mov_b32 s0, m0
	s_mov_b32 m0, s34
	s_nop 0
	global_load_lds_dwordx4 v[2:3], off
	s_mov_b32 m0, s0
	ds_read_b128 v[82:85], v211 offset:8192
	ds_read_b128 v[170:173], v211 offset:12288
	ds_read_b128 v[166:169], v210 offset:8192
	ds_read_b128 v[162:165], v210 offset:12288
	ds_read_b128 v[126:129], v209 offset:8192
	ds_read_b128 v[122:125], v209 offset:12288
	ds_read_b128 v[118:121], v208 offset:8192
	ds_read_b128 v[114:117], v208 offset:12288
	v_exp_f32_e32 v52, v4
	v_lshl_add_u64 v[2:3], s[16:17], 0, v[86:87]
	v_bitop3_b32 v4, v89, 7, v0 bitop3:0x48
	v_exp_f32_e32 v66, v18
	v_exp_f32_e32 v67, v19
	v_exp_f32_e32 v68, v20
	v_exp_f32_e32 v69, v21
	v_exp_f32_e32 v70, v22
	v_exp_f32_e32 v71, v23
	v_exp_f32_e32 v72, v24
	v_exp_f32_e32 v73, v25
	v_exp_f32_e32 v74, v26
	v_exp_f32_e32 v75, v27
	v_exp_f32_e32 v76, v28
	v_exp_f32_e32 v77, v29
	v_exp_f32_e32 v78, v30
	v_exp_f32_e32 v79, v31
	v_exp_f32_e32 v80, v32
	v_exp_f32_e32 v81, v33
	v_exp_f32_e32 v53, v5
	v_exp_f32_e32 v54, v6
	v_exp_f32_e32 v55, v7
	v_exp_f32_e32 v56, v8
	v_exp_f32_e32 v57, v9
	v_exp_f32_e32 v58, v10
	v_exp_f32_e32 v59, v11
	v_exp_f32_e32 v60, v12
	v_exp_f32_e32 v61, v13
	v_exp_f32_e32 v62, v14
	v_exp_f32_e32 v63, v15
	v_exp_f32_e32 v64, v16
	v_exp_f32_e32 v65, v17
	v_lshl_or_b32 v4, v4, 4, v2
	v_mov_b32_e32 v5, v3
	s_waitcnt vmcnt(2) lgkmcnt(0)
	s_barrier
	v_lshl_add_u64 v[4:5], s[4:5], 0, v[4:5]
	v_or_b32_e32 v2, v2, v182
	v_lshl_add_u64 v[188:189], v[4:5], 0, s[2:3]
	v_lshl_add_u64 v[2:3], s[4:5], 0, v[2:3]
	s_mov_b64 s[2:3], 0x2002000
	v_cmp_gt_u32_e64 s[0:1], 32, v90
	v_lshl_add_u64 v[196:197], v[2:3], 0, s[2:3]
	s_mov_b64 s[2:3], 0x8000
	v_mov_b32_e32 v2, v183
	v_mov_b32_e32 v3, v183
	v_mov_b32_e32 v4, v183
	v_mov_b32_e32 v5, v183
	v_mov_b32_e32 v6, v183
	v_mov_b32_e32 v7, v183
	v_mov_b32_e32 v8, v183
	v_mov_b32_e32 v9, v183
	v_mov_b32_e32 v10, v183
	v_mov_b32_e32 v11, v183
	v_mov_b32_e32 v12, v183
	v_mov_b32_e32 v13, v183
	v_mov_b32_e32 v14, v183
	v_mov_b32_e32 v15, v183
	v_mov_b32_e32 v16, v183
	v_mov_b32_e32 v17, v183
	v_mov_b32_e32 v18, v183
	v_mov_b32_e32 v19, v183
	v_mov_b32_e32 v20, v183
	v_mov_b32_e32 v21, v183
	v_mov_b32_e32 v22, v183
	v_mov_b32_e32 v23, v183
	v_mov_b32_e32 v24, v183
	v_mov_b32_e32 v25, v183
	v_mov_b32_e32 v26, v183
	v_mov_b32_e32 v27, v183
	v_mov_b32_e32 v28, v183
	v_mov_b32_e32 v29, v183
	v_mov_b32_e32 v30, v183
	v_mov_b32_e32 v31, v183
	v_mov_b32_e32 v32, v183
	v_mov_b32_e32 v33, v183
.LBB2_1:
	v_add_u32_e32 v130, s26, v206
	ds_read_b64_tr_b16 v[178:179], v130 offset:24576
	ds_read_b64_tr_b16 v[180:181], v130 offset:25600
	s_waitcnt lgkmcnt(9)
	v_mfma_f32_32x32x16_f16 v[98:113], v[82:85], v[154:157], v[34:49]
	v_add_f32_e32 v86, v66, v67
	v_add_f32_e32 v86, v68, v86
	v_add_f32_e32 v86, v69, v86
	v_add_f32_e32 v86, v70, v86
	v_add_f32_e32 v86, v71, v86
	v_cvt_pk_f16_f32 v158, v66, v67
	v_cvt_pk_f16_f32 v159, v68, v69
	v_add_u32_e32 v182, s26, v207
	ds_read_b64_tr_b16 v[174:175], v182 offset:24576
	ds_read_b64_tr_b16 v[176:177], v182 offset:25600
	v_add_f32_e32 v66, v72, v86
	s_waitcnt lgkmcnt(10)
	v_mfma_f32_32x32x16_f16 v[82:97], v[170:173], v[154:157], v[34:49]
	v_add_f32_e32 v66, v73, v66
	v_add_f32_e32 v66, v74, v66
	v_add_f32_e32 v66, v75, v66
	v_cvt_pk_f16_f32 v160, v70, v71
	v_cvt_pk_f16_f32 v161, v72, v73
	ds_read_b64_tr_b16 v[170:171], v130 offset:26624
	ds_read_b64_tr_b16 v[172:173], v130 offset:27648
	s_waitcnt lgkmcnt(11)
	v_mfma_f32_32x32x16_f16 v[98:113], v[166:169], v[146:149], v[98:113]
	v_add_f32_e32 v66, v76, v66
	v_add_f32_e32 v66, v77, v66
	v_add_f32_e32 v66, v78, v66
	v_add_f32_e32 v66, v79, v66
	v_cvt_pk_f16_f32 v150, v74, v75
	v_cvt_pk_f16_f32 v151, v76, v77
	ds_read_b64_tr_b16 v[74:75], v182 offset:26624
	ds_read_b64_tr_b16 v[76:77], v182 offset:27648
	s_waitcnt lgkmcnt(12)
	v_mfma_f32_32x32x16_f16 v[82:97], v[162:165], v[146:149], v[82:97]
	v_add_f32_e32 v66, v80, v66
	v_add_f32_e32 v66, v81, v66
	v_add_f32_e32 v66, v50, v66
	v_add_f32_e32 v66, v51, v66
	v_cvt_pk_f16_f32 v152, v78, v79
	v_cvt_pk_f16_f32 v153, v80, v81
	ds_read_b64_tr_b16 v[70:71], v130 offset:28672
	ds_read_b64_tr_b16 v[72:73], v130 offset:29696
	s_waitcnt lgkmcnt(13)
	v_mfma_f32_32x32x16_f16 v[98:113], v[126:129], v[138:141], v[98:113]
	v_add_f32_e32 v66, v52, v66
	v_add_f32_e32 v66, v53, v66
	v_add_f32_e32 v66, v54, v66
	v_add_f32_e32 v78, v55, v66
	v_cvt_pk_f16_f32 v142, v50, v51
	v_cvt_pk_f16_f32 v143, v52, v53
	ds_read_b64_tr_b16 v[66:67], v182 offset:28672
	ds_read_b64_tr_b16 v[68:69], v182 offset:29696
	s_waitcnt lgkmcnt(14)
	v_mfma_f32_32x32x16_f16 v[82:97], v[122:125], v[138:141], v[82:97]
	v_add_f32_e32 v50, v56, v78
	v_add_f32_e32 v50, v57, v50
	v_add_f32_e32 v50, v58, v50
	v_add_f32_e32 v50, v59, v50
	v_cvt_pk_f16_f32 v144, v54, v55
	v_cvt_pk_f16_f32 v145, v56, v57
	ds_read_b64_tr_b16 v[54:55], v130 offset:30720
	ds_read_b64_tr_b16 v[56:57], v130 offset:31744
	s_waitcnt lgkmcnt(14)
	v_mfma_f32_32x32x16_f16 v[98:113], v[118:121], v[134:137], v[98:113]
	v_add_f32_e32 v50, v60, v50
	v_add_f32_e32 v50, v61, v50
	v_add_f32_e32 v50, v62, v50
	v_add_f32_e32 v78, v63, v50
	v_cvt_pk_f16_f32 v130, v58, v59
	v_cvt_pk_f16_f32 v131, v60, v61
	ds_read_b64_tr_b16 v[50:51], v182 offset:30720
	ds_read_b64_tr_b16 v[52:53], v182 offset:31744
	v_mfma_f32_32x32x16_f16 v[82:97], v[114:117], v[134:137], v[82:97]
	v_add_f32_e32 v58, v64, v78
	v_add_f32_e32 v58, v65, v58
	v_add_f32_e32 v60, 0, v58
	v_cvt_pk_f16_f32 v132, v62, v63
	v_cvt_pk_f16_f32 v133, v64, v65
	v_lshl_add_u64 v[58:59], v[188:189], 0, s[24:25]
	s_add_i32 s26, s42, s36
	s_mov_b32 m0, s26
	s_nop 0
	global_load_lds_dwordx4 v[58:59], off
	v_lshl_add_u64 v[58:59], v[196:197], 0, s[20:21]
	s_add_i32 s26, s39, s35
	s_mov_b32 m0, s26
	s_nop 0
	global_load_lds_dwordx4 v[58:59], off
	v_max_f32_e32 v58, v98, v99
	v_max3_f32 v59, v100, v101, v83
	v_max3_f32 v58, v58, v82, v84
	v_max3_f32 v58, v58, v85, v102
	v_max3_f32 v59, v59, v104, v105
	v_max3_f32 v58, v58, v103, v86
	v_max3_f32 v59, v59, v88, v89
	v_max3_f32 v58, v58, v87, v106
	v_max3_f32 v59, v59, v108, v109
	v_max3_f32 v58, v58, v107, v90
	v_max3_f32 v59, v59, v92, v93
	v_max3_f32 v58, v58, v91, v110
	v_max3_f32 v59, v59, v112, v113
	v_max3_f32 v58, v58, v111, v94
	v_max3_f32 v59, v59, v96, v97
	v_max3_f32 v58, v58, v95, v59
	v_mov_b32_e32 v59, v58
	s_nop 1
	v_permlane32_swap_b32_e32 v58, v59
	v_max_f32_e32 v58, v58, v59
	v_cmp_lt_f32_e32 vcc, s41, v58
	s_cmp_lg_u64 vcc, 0
	v_add_f32_e32 v198, v183, v60
	s_cselect_b64 s[26:27], -1, 0
	s_cbranch_vccnz .LBB2_9

.LBB2_4:
	s_add_i32 s26, s39, 0x2000
	s_cmpk_lg_i32 s39, 0x4000
	s_cselect_b32 s43, s26, 0
	v_add_u32_e32 v130, s42, v206
	ds_read_b64_tr_b16 v[126:127], v130 offset:24576
	ds_read_b64_tr_b16 v[128:129], v130 offset:25600
	s_waitcnt lgkmcnt(9)
	v_mfma_f32_32x32x16_f16 v[66:81], v[58:61], v[154:157], v[34:49]
	v_add_f32_e32 v50, v98, v99
	v_add_f32_e32 v50, v100, v50
	v_add_f32_e32 v50, v101, v50
	v_add_f32_e32 v50, v102, v50
	v_add_f32_e32 v50, v103, v50
	v_cvt_pk_f16_f32 v158, v98, v99
	v_cvt_pk_f16_f32 v159, v100, v101
	v_add_u32_e32 v199, s42, v207
	ds_read_b64_tr_b16 v[122:123], v199 offset:24576
	ds_read_b64_tr_b16 v[124:125], v199 offset:25600
	v_add_f32_e32 v50, v104, v50
	v_add_f32_e32 v50, v105, v50
	v_add_f32_e32 v50, v106, v50
	v_add_f32_e32 v98, v107, v50
	s_waitcnt lgkmcnt(10)
	v_mfma_f32_32x32x16_f16 v[50:65], v[114:117], v[154:157], v[34:49]
	v_cvt_pk_f16_f32 v160, v102, v103
	v_cvt_pk_f16_f32 v161, v104, v105
	ds_read_b64_tr_b16 v[118:119], v130 offset:26624
	ds_read_b64_tr_b16 v[120:121], v130 offset:27648
	s_waitcnt lgkmcnt(11)
	v_mfma_f32_32x32x16_f16 v[66:81], v[182:185], v[146:149], v[66:81]
	v_add_f32_e32 v98, v108, v98
	v_add_f32_e32 v98, v109, v98
	v_add_f32_e32 v98, v110, v98
	v_add_f32_e32 v98, v111, v98
	v_cvt_pk_f16_f32 v150, v106, v107
	v_cvt_pk_f16_f32 v151, v108, v109
	ds_read_b64_tr_b16 v[114:115], v199 offset:26624
	ds_read_b64_tr_b16 v[116:117], v199 offset:27648
	s_waitcnt lgkmcnt(12)
	v_mfma_f32_32x32x16_f16 v[50:65], v[174:177], v[146:149], v[50:65]
	v_add_f32_e32 v98, v112, v98
	v_add_f32_e32 v98, v113, v98
	v_add_f32_e32 v98, v82, v98
	v_add_f32_e32 v98, v83, v98
	v_cvt_pk_f16_f32 v152, v110, v111
	v_cvt_pk_f16_f32 v153, v112, v113
	ds_read_b64_tr_b16 v[106:107], v130 offset:28672
	ds_read_b64_tr_b16 v[108:109], v130 offset:29696
	s_waitcnt lgkmcnt(13)
	v_mfma_f32_32x32x16_f16 v[66:81], v[178:181], v[138:141], v[66:81]
	v_add_f32_e32 v98, v84, v98
	v_add_f32_e32 v98, v85, v98
	v_add_f32_e32 v98, v86, v98
	v_add_f32_e32 v98, v87, v98
	v_cvt_pk_f16_f32 v142, v82, v83
	v_cvt_pk_f16_f32 v143, v84, v85
	ds_read_b64_tr_b16 v[102:103], v199 offset:28672
	ds_read_b64_tr_b16 v[104:105], v199 offset:29696
	s_waitcnt lgkmcnt(14)
	v_mfma_f32_32x32x16_f16 v[50:65], v[166:169], v[138:141], v[50:65]
	v_add_f32_e32 v82, v88, v98
	v_add_f32_e32 v82, v89, v82
	v_add_f32_e32 v82, v90, v82
	v_add_f32_e32 v82, v91, v82
	v_cvt_pk_f16_f32 v144, v86, v87
	v_cvt_pk_f16_f32 v145, v88, v89
	ds_read_b64_tr_b16 v[98:99], v130 offset:30720
	ds_read_b64_tr_b16 v[100:101], v130 offset:31744
	s_waitcnt lgkmcnt(14)
	v_mfma_f32_32x32x16_f16 v[66:81], v[170:173], v[134:137], v[66:81]
	v_add_f32_e32 v82, v92, v82
	v_add_f32_e32 v82, v93, v82
	v_add_f32_e32 v82, v94, v82
	v_add_f32_e32 v82, v95, v82
	v_cvt_pk_f16_f32 v130, v90, v91
	v_cvt_pk_f16_f32 v131, v92, v93
	ds_read_b64_tr_b16 v[86:87], v199 offset:30720
	ds_read_b64_tr_b16 v[88:89], v199 offset:31744
	v_mfma_f32_32x32x16_f16 v[50:65], v[162:165], v[134:137], v[50:65]
	v_add_f32_e32 v82, v96, v82
	v_add_f32_e32 v82, v97, v82
	v_add_f32_e32 v84, 0, v82
	v_cvt_pk_f16_f32 v132, v94, v95
	v_cvt_pk_f16_f32 v133, v96, v97
	v_lshl_add_u64 v[82:83], v[188:189], 0, s[2:3]
	s_add_i32 s26, s39, s36
	s_mov_b32 m0, s26
	s_nop 0
	global_load_lds_dwordx4 v[82:83], off
	v_max_f32_e32 v82, v66, v67
	s_nop 1
	v_max3_f32 v83, v68, v69, v51
	v_max3_f32 v82, v82, v50, v52
	v_max3_f32 v82, v82, v53, v70
	v_max3_f32 v83, v83, v72, v73
	v_max3_f32 v82, v82, v71, v54
	v_max3_f32 v83, v83, v56, v57
	v_max3_f32 v82, v82, v55, v74
	v_max3_f32 v83, v83, v76, v77
	v_max3_f32 v82, v82, v75, v58
	v_max3_f32 v83, v83, v60, v61
	v_max3_f32 v82, v82, v59, v78
	v_max3_f32 v83, v83, v80, v81
	v_max3_f32 v82, v82, v79, v62
	v_max3_f32 v83, v83, v64, v65
	v_max3_f32 v82, v82, v63, v83
	v_mov_b32_e32 v83, v82
	s_nop 1
	v_permlane32_swap_b32_e32 v82, v83
	v_max_f32_e32 v82, v82, v83
	v_lshl_add_u64 v[196:197], v[196:197], 0, s[22:23]
	s_add_i32 s26, s43, s35
	s_mov_b32 m0, s26
	s_nop 0
	global_load_lds_dwordx4 v[196:197], off
	v_cmp_lt_f32_e32 vcc, s41, v82
	s_cmp_lg_u64 vcc, 0
	v_add_f32_e32 v183, v198, v84
	s_cselect_b64 s[26:27], -1, 0
	s_cbranch_vccnz .LBB2_12

.LBB2_30:
	v_add_f32_e32 v50, v66, v67
	v_add_f32_e32 v50, v68, v50
	v_add_f32_e32 v50, v69, v50
	v_add_f32_e32 v50, v70, v50
	v_add_f32_e32 v50, v71, v50
	v_add_f32_e32 v50, v72, v50
	v_add_f32_e32 v50, v73, v50
	v_add_f32_e32 v50, v74, v50
	v_add_f32_e32 v50, v75, v50
	v_add_f32_e32 v50, v76, v50
	v_add_f32_e32 v50, v77, v50
	v_add_f32_e32 v50, v78, v50
	v_add_f32_e32 v50, v79, v50
	v_add_f32_e32 v50, v80, v50
	v_add_f32_e32 v50, v81, v50
	v_add_f32_e32 v50, v34, v50
	v_add_f32_e32 v50, v35, v50
	v_add_f32_e32 v50, v36, v50
	v_add_f32_e32 v50, v37, v50
	v_add_f32_e32 v50, v38, v50
	v_add_f32_e32 v50, v39, v50
	v_add_f32_e32 v50, v40, v50
	v_add_f32_e32 v50, v41, v50
	v_add_f32_e32 v50, v42, v50
	v_add_f32_e32 v50, v43, v50
	v_add_f32_e32 v50, v44, v50
	v_add_f32_e32 v50, v45, v50
	v_add_f32_e32 v50, v46, v50
	v_add_f32_e32 v50, v47, v50
	v_add_f32_e32 v50, v48, v50
	v_add_f32_e32 v50, v49, v50
	v_add_f32_e32 v50, v86, v50
	v_cvt_pk_f16_f32 v34, v34, v35
	v_cvt_pk_f16_f32 v52, v66, v67
	v_cvt_pk_f16_f32 v53, v68, v69
	v_cvt_pk_f16_f32 v54, v70, v71
	v_cvt_pk_f16_f32 v55, v72, v73
	v_cvt_pk_f16_f32 v56, v74, v75
	v_cvt_pk_f16_f32 v57, v76, v77
	v_cvt_pk_f16_f32 v58, v78, v79
	v_cvt_pk_f16_f32 v59, v80, v81
	v_cvt_pk_f16_f32 v35, v36, v37
	v_cvt_pk_f16_f32 v36, v38, v39
	v_cvt_pk_f16_f32 v37, v40, v41
	v_cvt_pk_f16_f32 v38, v42, v43
	v_cvt_pk_f16_f32 v39, v44, v45
	v_cvt_pk_f16_f32 v40, v46, v47
	v_cvt_pk_f16_f32 v41, v48, v49
	v_or_b32_e32 v42, 0x8000, v203
	v_add_u32_e32 v199, v42, v200
	v_add_u32_e32 v197, v42, v202
	ds_read_b64_tr_b16 v[42:43],v199 offset:0
	ds_read_b64_tr_b16 v[44:45],v199 offset:1024
	ds_read_b64_tr_b16 v[46:47],v199 offset:2048
	ds_read_b64_tr_b16 v[48:49],v199 offset:3072
	ds_read_b64_tr_b16 v[60:61],v199 offset:4096
	ds_read_b64_tr_b16 v[62:63],v199 offset:5120
	ds_read_b64_tr_b16 v[64:65],v199 offset:6144
	ds_read_b64_tr_b16 v[66:67],v199 offset:7168
	s_waitcnt lgkmcnt(0)
	s_nop 0
	v_mfma_f32_32x32x16_f16 v[2:17], v[52:55], v[42:45], v[2:17]
	ds_read_b64_tr_b16 v[42:43],v197 offset:0
	ds_read_b64_tr_b16 v[44:45],v197 offset:1024
	v_mfma_f32_32x32x16_f16 v[2:17], v[56:59], v[46:49], v[2:17]
	ds_read_b64_tr_b16 v[46:47],v197 offset:2048
	ds_read_b64_tr_b16 v[48:49],v197 offset:3072
	v_mfma_f32_32x32x16_f16 v[2:17], v[34:37], v[60:63], v[2:17]
	ds_read_b64_tr_b16 v[60:61],v197 offset:4096
	ds_read_b64_tr_b16 v[62:63],v197 offset:5120
	ds_read_b64_tr_b16 v[68:69],v197 offset:6144
	ds_read_b64_tr_b16 v[70:71],v197 offset:7168
	s_waitcnt lgkmcnt(0)
	v_mfma_f32_32x32x16_f16 v[2:17], v[38:41], v[64:67], v[2:17]
	v_mfma_f32_32x32x16_f16 v[18:33], v[52:55], v[42:45], v[18:33]
	v_mfma_f32_32x32x16_f16 v[18:33], v[56:59], v[46:49], v[18:33]
	v_mfma_f32_32x32x16_f16 v[18:33], v[34:37], v[60:63], v[18:33]
	v_mov_b32_e32 v34, v50
	s_nop 1
	v_permlane32_swap_b32_e32 v50, v34
	v_mfma_f32_32x32x16_f16 v[18:33], v[38:41], v[68:71], v[18:33]
	s_and_saveexec_b64 s[2:3], s[0:1]
	v_add_f32_e32 v34, v50, v34
	ds_write_b32 v204, v34 offset:49280
	s_or_b64 exec, exec, s[2:3]
	s_waitcnt lgkmcnt(0)
	ds_read_b128 v[34:37], v213 offset:49280
	ds_read_b128 v[38:41], v213 offset:49312
	s_lshl_b32 s20, s33, 12
	v_or_b32_e32 v50, s20, v201
	v_lshl_add_u32 v50, v191, 1, v50
	s_waitcnt lgkmcnt(1)
	v_rcp_f32_e32 v42, v34
	v_rcp_f32_e32 v43, v35
	v_rcp_f32_e32 v44, v36
	v_rcp_f32_e32 v45, v37
	v_fma_mixlo_f16 v2, v2, v42, 0
	ds_write_b16 v50, v2 offset:51200
	v_fma_mixlo_f16 v2, v18, v42, 0
	ds_write_b16 v50, v2 offset:51264
	v_fma_mixlo_f16 v2, v3, v43, 0
	ds_write_b16 v50, v2 offset:51328
	v_fma_mixlo_f16 v2, v19, v43, 0
	s_waitcnt lgkmcnt(3)
	v_rcp_f32_e32 v46, v38
	ds_write_b16 v50, v2 offset:51392
	v_fma_mixlo_f16 v2, v4, v44, 0
	ds_write_b16 v50, v2 offset:51456
	v_fma_mixlo_f16 v2, v20, v44, 0
	v_rcp_f32_e32 v47, v39
	ds_write_b16 v50, v2 offset:51520
	v_fma_mixlo_f16 v2, v5, v45, 0
	ds_read_b128 v[34:37], v213 offset:49344
	ds_write_b16 v50, v2 offset:51584
	v_fma_mixlo_f16 v2, v21, v45, 0
	v_rcp_f32_e32 v48, v40
	ds_write_b16 v50, v2 offset:51648
	v_fma_mixlo_f16 v2, v6, v46, 0
	ds_write_b16 v50, v2 offset:52224
	v_fma_mixlo_f16 v2, v22, v46, 0
	v_rcp_f32_e32 v49, v41
	ds_write_b16 v50, v2 offset:52288
	v_fma_mixlo_f16 v2, v7, v47, 0
	ds_write_b16 v50, v2 offset:52352
	v_fma_mixlo_f16 v2, v23, v47, 0
	ds_read_b128 v[38:41], v213 offset:49376
	s_waitcnt lgkmcnt(6)
	v_rcp_f32_e32 v34, v34
	ds_write_b16 v50, v2 offset:52416
	v_fma_mixlo_f16 v2, v8, v48, 0
	ds_write_b16 v50, v2 offset:52480
	v_fma_mixlo_f16 v2, v24, v48, 0
	v_rcp_f32_e32 v35, v35
	ds_write_b16 v50, v2 offset:52544
	v_fma_mixlo_f16 v2, v9, v49, 0
	ds_write_b16 v50, v2 offset:52608
	v_fma_mixlo_f16 v2, v25, v49, 0
	v_rcp_f32_e32 v36, v36
	ds_write_b16 v50, v2 offset:52672
	v_fma_mixlo_f16 v2, v10, v34, 0
	ds_write_b16 v50, v2 offset:53248
	v_fma_mixlo_f16 v2, v26, v34, 0
	v_rcp_f32_e32 v37, v37
	ds_write_b16 v50, v2 offset:53312
	v_fma_mixlo_f16 v2, v11, v35, 0
	ds_write_b16 v50, v2 offset:53376
	v_fma_mixlo_f16 v2, v27, v35, 0
	s_waitcnt lgkmcnt(8)
	v_rcp_f32_e32 v38, v38
	ds_write_b16 v50, v2 offset:53440
	v_fma_mixlo_f16 v2, v12, v36, 0
	ds_write_b16 v50, v2 offset:53504
	v_fma_mixlo_f16 v2, v28, v36, 0
	v_rcp_f32_e32 v39, v39
	ds_write_b16 v50, v2 offset:53568
	v_fma_mixlo_f16 v2, v13, v37, 0
	ds_write_b16 v50, v2 offset:53632
	v_fma_mixlo_f16 v2, v29, v37, 0
	v_rcp_f32_e32 v40, v40
	ds_write_b16 v50, v2 offset:53696
	v_fma_mixlo_f16 v2, v14, v38, 0
	ds_write_b16 v50, v2 offset:54272
	v_fma_mixlo_f16 v2, v30, v38, 0
	v_rcp_f32_e32 v41, v41
	ds_write_b16 v50, v2 offset:54336
	v_fma_mixlo_f16 v2, v15, v39, 0
	ds_write_b16 v50, v2 offset:54400
	v_fma_mixlo_f16 v2, v31, v39, 0
	ds_write_b16 v50, v2 offset:54464
	v_fma_mixlo_f16 v2, v16, v40, 0
	ds_write_b16 v50, v2 offset:54528
	v_fma_mixlo_f16 v2, v32, v40, 0
	ds_write_b16 v50, v2 offset:54592
	v_fma_mixlo_f16 v2, v17, v41, 0
	s_lshl_b64 s[2:3], s[18:19], 11
	ds_write_b16 v50, v2 offset:54656
	v_fma_mixlo_f16 v2, v33, v41, 0
	ds_write_b16 v50, v2 offset:54720
	s_or_b64 s[18:19], s[2:3], s[12:13]
	v_lshlrev_b32_e32 v2, 11, v0
	v_lshlrev_b32_e32 v213, 4, v1
	v_and_b32_e32 v2, 0x2000, v2
	v_mov_b32_e32 v195, 0
	s_add_u32 s18, s31, s18
	v_or_b32_e32 v14, s20, v213
	v_lshl_or_b32 v194, s30, 14, v2
	s_addc_u32 s19, 0, s19
	v_lshlrev_b32_e32 v2, 1, v193
	v_mov_b32_e32 v3, v195
	v_lshlrev_b32_e32 v214, 7, v190
	s_waitcnt lgkmcnt(0)
	v_lshl_add_u64 v[10:11], s[18:19], 0, v[194:195]
	v_lshl_add_u64 v[188:189], s[6:7], 0, v[2:3]
	v_or_b32_e32 v2, v14, v214
	ds_read_b128 v[2:5], v2 offset:51200
	v_or_b32_e32 v6, v10, v190
	v_mov_b32_e32 v7, v11
	v_or_b32_e32 v196, 8, v190
	v_lshlrev_b64 v[6:7], 6, v[6:7]
	v_lshlrev_b32_e32 v215, 7, v196
	v_lshl_add_u64 v[12:13], v[188:189], 0, v[6:7]
	v_or_b32_e32 v6, v14, v215
	ds_read_b128 v[6:9], v6 offset:51200
	s_waitcnt lgkmcnt(1)
	global_store_dwordx4 v[12:13], v[2:5], off sc1
	v_or_b32_e32 v198, 16, v190
	v_lshlrev_b32_e32 v216, 7, v198
	v_or_b32_e32 v2, v10, v196
	v_mov_b32_e32 v3, v11
	v_lshlrev_b64 v[2:3], 6, v[2:3]
	v_lshl_add_u64 v[2:3], v[188:189], 0, v[2:3]
	s_waitcnt lgkmcnt(0)
	global_store_dwordx4 v[2:3], v[6:9], off sc1
	v_or_b32_e32 v2, v14, v216
	v_or_b32_e32 v200, 24, v190
	v_or_b32_e32 v6, v10, v198
	v_mov_b32_e32 v7, v11
	ds_read_b128 v[2:5], v2 offset:51200
	v_lshlrev_b64 v[6:7], 6, v[6:7]
	v_lshlrev_b32_e32 v217, 7, v200
	v_lshl_add_u64 v[12:13], v[188:189], 0, v[6:7]
	v_or_b32_e32 v6, v14, v217
	ds_read_b128 v[6:9], v6 offset:51200
	v_or_b32_e32 v10, v10, v200
	s_waitcnt lgkmcnt(1)
	global_store_dwordx4 v[12:13], v[2:5], off sc1
	v_readfirstlane_b32 s20, v0
	s_lshr_b32 s19, s20, 6
	v_lshlrev_b64 v[2:3], 6, v[10:11]
	v_lshl_add_u64 v[2:3], v[188:189], 0, v[2:3]
	s_waitcnt lgkmcnt(0)
	global_store_dwordx4 v[2:3], v[6:9], off sc1
	v_lshl_or_b32 v2, s19, 3, v190
	s_xor_b32 s6, s12, 0x700
	v_mov_b32_e32 v3, v195
	v_lshrrev_b32_e32 v88, 1, v2
	s_or_b32 s7, s8, s6
	s_lshl_b32 s18, s19, 5
	v_lshlrev_b64 v[84:85], 7, v[2:3]
	v_xor_b32_e32 v2, v88, v0
	s_add_u32 s8, s7, s18
	v_lshlrev_b32_e32 v2, 4, v2
	s_addc_u32 s9, s9, 0
	v_lshl_add_u64 v[4:5], s[14:15], 0, v[84:85]
	v_and_b32_e32 v2, 0x70, v2
	s_lshl_b64 s[8:9], s[8:9], 7
	v_lshl_add_u64 v[184:185], v[4:5], 0, v[2:3]
	v_lshlrev_b32_e32 v4, 1, v190
	s_waitcnt lgkmcnt(0)
	s_barrier
	s_cmp_lg_u32 s91, 0
	s_cbranch_scc1 .Lattn_done
	s_movk_i32 s91, 0x700
	s_mov_b64 s[0:1], s[88:89]
	s_mov_b32 s2, s87
	s_branch .Lattn_unit
.Lattn_done:
	s_endpgm
.LBB2_65:
	v_max_f32_e32 v34, v58, v58
	v_max_f32_e32 v48, 0, v34
	v_exp_f32_e64 v58, -v48
	v_add_f32_e32 v205, v205, v48
	v_xor_b32_e32 v34, 0x80000000, v205
	v_sub_f32_e32 v113, v113, v48
	v_sub_f32_e32 v112, v112, v48
	v_sub_f32_e32 v111, v111, v48
	v_sub_f32_e32 v110, v110, v48
	v_sub_f32_e32 v109, v109, v48
	v_sub_f32_e32 v108, v108, v48
	v_sub_f32_e32 v107, v107, v48
	v_sub_f32_e32 v106, v106, v48
	v_sub_f32_e32 v105, v105, v48
	v_sub_f32_e32 v104, v104, v48
	v_sub_f32_e32 v103, v103, v48
	v_sub_f32_e32 v102, v102, v48
	v_sub_f32_e32 v101, v101, v48
	v_sub_f32_e32 v100, v100, v48
	v_sub_f32_e32 v99, v99, v48
	v_sub_f32_e32 v98, v98, v48
	v_sub_f32_e32 v97, v97, v48
	v_sub_f32_e32 v96, v96, v48
	v_sub_f32_e32 v95, v95, v48
	v_sub_f32_e32 v94, v94, v48
	v_sub_f32_e32 v93, v93, v48
	v_sub_f32_e32 v92, v92, v48
	v_sub_f32_e32 v91, v91, v48
	v_sub_f32_e32 v90, v90, v48
	v_sub_f32_e32 v89, v89, v48
	v_sub_f32_e32 v88, v88, v48
	v_sub_f32_e32 v87, v87, v48
	v_sub_f32_e32 v86, v86, v48
	v_sub_f32_e32 v85, v85, v48
	v_sub_f32_e32 v84, v84, v48
	v_sub_f32_e32 v83, v83, v48
	v_sub_f32_e32 v82, v82, v48
	v_mov_b32_e32 v35, v34
	v_mov_b32_e32 v36, v34
	v_mov_b32_e32 v37, v34
	v_mov_b32_e32 v38, v34
	v_mov_b32_e32 v39, v34
	v_mov_b32_e32 v40, v34
	v_mov_b32_e32 v41, v34
	v_mov_b32_e32 v42, v34
	v_mov_b32_e32 v43, v34
	v_mov_b32_e32 v44, v34
	v_mov_b32_e32 v45, v34
	v_mov_b32_e32 v46, v34
	v_mov_b32_e32 v47, v34
	v_mov_b32_e32 v48, v34
	v_mov_b32_e32 v49, v34
	s_and_saveexec_b64 s[22:23], s[0:1]
	ds_write_b32 v204, v58 offset:49152
	s_or_b64 exec, exec, s[22:23]
	v_mul_f32_e32 v214, v214, v58
	s_branch .LBB2_16

.LBB2_77:
	v_max_f32_e32 v50, v50, v50
	v_max_f32_e32 v64, 0, v50
	v_exp_f32_e64 v87, -v64
	v_add_f32_e32 v50, v205, v64
	v_xor_b32_e32 v50, 0x80000000, v50
	v_sub_f32_e32 v81, v81, v64
	v_sub_f32_e32 v80, v80, v64
	v_sub_f32_e32 v79, v79, v64
	v_sub_f32_e32 v78, v78, v64
	v_sub_f32_e32 v77, v77, v64
	v_sub_f32_e32 v76, v76, v64
	v_sub_f32_e32 v75, v75, v64
	v_sub_f32_e32 v74, v74, v64
	v_sub_f32_e32 v73, v73, v64
	v_sub_f32_e32 v72, v72, v64
	v_sub_f32_e32 v71, v71, v64
	v_sub_f32_e32 v70, v70, v64
	v_sub_f32_e32 v69, v69, v64
	v_sub_f32_e32 v68, v68, v64
	v_sub_f32_e32 v67, v67, v64
	v_sub_f32_e32 v66, v66, v64
	v_sub_f32_e32 v49, v49, v64
	v_sub_f32_e32 v48, v48, v64
	v_sub_f32_e32 v47, v47, v64
	v_sub_f32_e32 v46, v46, v64
	v_sub_f32_e32 v45, v45, v64
	v_sub_f32_e32 v44, v44, v64
	v_sub_f32_e32 v43, v43, v64
	v_sub_f32_e32 v42, v42, v64
	v_sub_f32_e32 v41, v41, v64
	v_sub_f32_e32 v40, v40, v64
	v_sub_f32_e32 v39, v39, v64
	v_sub_f32_e32 v38, v38, v64
	v_sub_f32_e32 v37, v37, v64
	v_sub_f32_e32 v36, v36, v64
	v_sub_f32_e32 v35, v35, v64
	v_sub_f32_e32 v34, v34, v64
	v_mov_b32_e32 v51, v50
	v_mov_b32_e32 v52, v50
	v_mov_b32_e32 v53, v50
	v_mov_b32_e32 v54, v50
	v_mov_b32_e32 v55, v50
	v_mov_b32_e32 v56, v50
	v_mov_b32_e32 v57, v50
	v_mov_b32_e32 v58, v50
	v_mov_b32_e32 v59, v50
	v_mov_b32_e32 v60, v50
	v_mov_b32_e32 v61, v50
	v_mov_b32_e32 v62, v50
	v_mov_b32_e32 v63, v50
	v_mov_b32_e32 v64, v50
	v_mov_b32_e32 v65, v50
	s_and_saveexec_b64 s[20:21], s[0:1]
	ds_write_b32 v204, v87 offset:49152
	s_or_b64 exec, exec, s[20:21]
	v_mul_f32_e32 v86, v86, v87
	s_branch .LBB2_28
	.section	.rodata,"a",@progbits
	.p2align	6, 0x0
